# grid barrier: acquire invalidate issued at arrival instead of after release
# speedup vs baseline: 1.0068x; 1.0035x over previous
.LBB0_139:
	v_readlane_b32 s6, v255, 4
	v_readlane_b32 s7, v255, 5
	s_lshl_b64 s[6:7], s[6:7], 2
	v_readlane_b32 s3, v255, 2
	s_add_u32 s8, s3, s6
	v_readlane_b32 s3, v255, 3
	s_addc_u32 s9, s3, s7
	v_readlane_b32 s3, v255, 6
	s_lshl_b32 s3, s3, 8
	s_add_u32 s6, s8, s3
	s_addc_u32 s7, s9, 0
	v_mov_b32_e32 v2, 0x1000
	v_mov_b32_e32 v4, 1
	buffer_inv sc1
	global_atomic_add v4, v2, v4, s[6:7] offset:1024 sc0
	v_cvt_f32_u32_e32 v2, v3
	v_sub_u32_e32 v5, 0, v3
	v_rcp_iflag_f32_e32 v2, v2
	s_nop 0
	v_mul_f32_e32 v2, 0x4f7ffffe, v2
	v_cvt_u32_f32_e32 v2, v2
	v_mul_lo_u32 v5, v5, v2
	v_mul_hi_u32 v5, v2, v5
	v_add_u32_e32 v2, v2, v5
	s_waitcnt vmcnt(0)
	v_mul_hi_u32 v2, v4, v2
	v_mul_lo_u32 v5, v2, v3
	v_sub_u32_e32 v5, v4, v5
	v_add_u32_e32 v6, 1, v2
	v_cmp_ge_u32_e32 vcc, v5, v3
	v_add_u32_e32 v4, 1, v4
	s_nop 0
	v_cndmask_b32_e32 v2, v2, v6, vcc
	v_sub_u32_e32 v6, v5, v3
	v_cndmask_b32_e32 v5, v5, v6, vcc
	v_add_u32_e32 v6, 1, v2
	v_cmp_ge_u32_e32 vcc, v5, v3
	s_nop 1
	v_cndmask_b32_e32 v2, v2, v6, vcc
	v_mul_lo_u32 v5, v3, v2
	v_add_u32_e32 v3, v5, v3
	v_cmp_ne_u32_e32 vcc, v4, v3
	s_and_saveexec_b64 s[12:13], vcc
	s_xor_b64 s[12:13], exec, s[12:13]
	s_cbranch_execz .LBB0_153
	s_waitcnt lgkmcnt(0)
	v_mov_b32_e32 v1, 0x2000
	global_load_dword v1, v1, s[6:7] offset:1024 sc1
	s_add_u32 s16, s6, 0x2400
	s_addc_u32 s17, s7, 0
	s_waitcnt vmcnt(0)
	v_cmp_eq_u32_e32 vcc, v1, v2
	s_and_saveexec_b64 s[14:15], vcc
	s_cbranch_execz .LBB0_152
	s_mov_b32 s3, 1
	s_mov_b64 s[18:19], 0
	v_mov_b32_e32 v1, 0
	s_branch .LBB0_143

.LBB0_152:
	s_or_b64 exec, exec, s[14:15]
	s_waitcnt vmcnt(0)
	s_waitcnt vmcnt(0)

.LBB0_170:
	s_or_b64 exec, exec, s[8:9]
	v_mov_b32_e32 v1, 0x2000
	v_mov_b32_e32 v2, 1
	s_waitcnt vmcnt(0)
	global_atomic_add v1, v2, s[6:7] offset:1024
	s_waitcnt vmcnt(0)

.LBB0_193:
	v_readlane_b32 s6, v255, 4
	v_readlane_b32 s7, v255, 5
	s_lshl_b64 s[6:7], s[6:7], 2
	v_readlane_b32 s3, v255, 2
	s_add_u32 s8, s3, s6
	v_readlane_b32 s3, v255, 3
	s_addc_u32 s9, s3, s7
	v_readlane_b32 s3, v255, 6
	s_lshl_b32 s3, s3, 8
	s_add_u32 s6, s8, s3
	s_addc_u32 s7, s9, 0
	v_mov_b32_e32 v2, 0x1000
	v_mov_b32_e32 v4, 1
	buffer_inv sc1
	global_atomic_add v4, v2, v4, s[6:7] offset:1024 sc0
	v_cvt_f32_u32_e32 v2, v3
	v_sub_u32_e32 v5, 0, v3
	v_rcp_iflag_f32_e32 v2, v2
	s_nop 0
	v_mul_f32_e32 v2, 0x4f7ffffe, v2
	v_cvt_u32_f32_e32 v2, v2
	v_mul_lo_u32 v5, v5, v2
	v_mul_hi_u32 v5, v2, v5
	v_add_u32_e32 v2, v2, v5
	s_waitcnt vmcnt(0)
	v_mul_hi_u32 v2, v4, v2
	v_mul_lo_u32 v5, v2, v3
	v_sub_u32_e32 v5, v4, v5
	v_add_u32_e32 v6, 1, v2
	v_cmp_ge_u32_e32 vcc, v5, v3
	v_add_u32_e32 v4, 1, v4
	s_nop 0
	v_cndmask_b32_e32 v2, v2, v6, vcc
	v_sub_u32_e32 v6, v5, v3
	v_cndmask_b32_e32 v5, v5, v6, vcc
	v_add_u32_e32 v6, 1, v2
	v_cmp_ge_u32_e32 vcc, v5, v3
	s_nop 1
	v_cndmask_b32_e32 v2, v2, v6, vcc
	v_mul_lo_u32 v5, v3, v2
	v_add_u32_e32 v3, v5, v3
	v_cmp_ne_u32_e32 vcc, v4, v3
	s_and_saveexec_b64 s[10:11], vcc
	s_xor_b64 s[10:11], exec, s[10:11]
	s_cbranch_execz .LBB0_207
	s_waitcnt lgkmcnt(0)
	v_mov_b32_e32 v1, 0x2000
	global_load_dword v1, v1, s[6:7] offset:1024 sc1
	s_add_u32 s14, s6, 0x2400
	s_addc_u32 s15, s7, 0
	s_waitcnt vmcnt(0)
	v_cmp_eq_u32_e32 vcc, v1, v2
	s_and_saveexec_b64 s[12:13], vcc
	s_cbranch_execz .LBB0_206
	s_mov_b32 s3, 1
	s_mov_b64 s[16:17], 0
	v_mov_b32_e32 v1, 0
	s_branch .LBB0_197

.LBB0_206:
	s_or_b64 exec, exec, s[12:13]
	s_waitcnt vmcnt(0)
	s_waitcnt vmcnt(0)

.LBB0_1173:
	s_mul_hi_u32 s7, s80, 0xaaaaaaab
	s_lshr_b32 s7, s7, 1
	s_mul_i32 s7, s7, 0xfffee000
	v_add_u32_e32 v166, s6, v159
	v_add_u32_e32 v167, s6, v161
	v_add_u32_e32 v185, s6, v162
	v_add_u32_e32 v230, s6, v163
	ds_read_b128 v[66:69], v166 offset:32768
	ds_read_b128 v[82:85], v167 offset:32768
	ds_read_b128 v[86:89], v185 offset:32768
	ds_read_b128 v[90:93], v230 offset:32768
	ds_read_b128 v[94:97], v166 offset:32896
	ds_read_b128 v[186:189], v167 offset:32896
	ds_read_b128 v[190:193], v185 offset:32896
	ds_read_b128 v[194:197], v230 offset:32896
	ds_read_b128 v[198:201], v158
	ds_read_b128 v[202:205], v166 offset:33024
	ds_read_b128 v[206:209], v158 offset:1024
	ds_read_b128 v[210:213], v167 offset:33024
	ds_read_b128 v[214:217], v158 offset:2048
	ds_read_b128 v[218:221], v185 offset:33024
	ds_read_b128 v[222:225], v158 offset:3072
	s_waitcnt lgkmcnt(14)
	v_mfma_f32_32x32x16_bf16 v[66:81], v[66:69], v[126:129], 0
	ds_read_b128 v[226:229], v230 offset:33024
	s_waitcnt lgkmcnt(11)
	v_mfma_f32_32x32x16_bf16 v[66:81], v[82:85], v[122:125], v[66:81]
	v_mfma_f32_32x32x16_bf16 v[66:81], v[86:89], v[118:121], v[66:81]
	v_mfma_f32_32x32x16_bf16 v[66:81], v[90:93], v[114:117], v[66:81]
	v_mfma_f32_32x32x16_bf16 v[66:81], v[94:97], v[110:113], v[66:81]
	s_waitcnt lgkmcnt(8)
	v_mfma_f32_32x32x16_bf16 v[66:81], v[186:189], v[106:109], v[66:81]
	ds_read_b128 v[186:189], v166 offset:45056
	v_mfma_f32_32x32x16_bf16 v[66:81], v[190:193], v[102:105], v[66:81]
	ds_read_b128 v[190:193], v167 offset:45056
	v_mfma_f32_32x32x16_bf16 v[66:81], v[194:197], v[98:101], v[66:81]
	ds_read_b128 v[194:197], v185 offset:45056
	s_waitcnt lgkmcnt(3)
	v_mfma_f32_32x32x16_bf16 v[66:81], v[202:205], v[198:201], v[66:81]
	ds_read_b128 v[202:205], v230 offset:45056
	v_mfma_f32_32x32x16_bf16 v[66:81], v[210:213], v[206:209], v[66:81]
	ds_read_b128 v[210:213], v166 offset:45184
	v_mfma_f32_32x32x16_bf16 v[66:81], v[218:221], v[214:217], v[66:81]
	ds_read_b128 v[218:221], v167 offset:45184
	v_mfma_f32_32x32x16_bf16 v[66:81], v[226:229], v[222:225], v[66:81]
	ds_read_b128 v[226:229], v185 offset:45184
	s_waitcnt lgkmcnt(3)
	v_mfma_f32_32x32x16_bf16 v[82:97], v[186:189], v[126:129], 0
	ds_read_b128 v[186:189], v230 offset:45184
	s_add_i32 s6, s78, 1
	s_min_u32 s6, s6, s14
	v_mfma_f32_32x32x16_bf16 v[82:97], v[190:193], v[122:125], v[82:97]
	ds_read_b128 v[246:249], v166 offset:45312
	s_lshl_b32 s10, s6, 6
	v_mfma_f32_32x32x16_bf16 v[82:97], v[194:197], v[118:121], v[82:97]
	ds_read_b128 v[242:245], v167 offset:45312
	s_cmp_lt_u32 s6, 4
	s_cselect_b32 s6, s74, s15
	s_add_i32 s6, s6, s10
	v_mfma_f32_32x32x16_bf16 v[82:97], v[202:205], v[114:117], v[82:97]
	ds_read_b128 v[238:241], v185 offset:45312
	s_mul_hi_i32 s11, s6, 0x1080
	s_mulk_i32 s6, 0x1080
	s_waitcnt lgkmcnt(3)
	v_mfma_f32_32x32x16_bf16 v[82:97], v[210:213], v[110:113], v[82:97]
	ds_read_b128 v[234:237], v230 offset:45312
	s_add_u32 s10, s3, s6
	s_addc_u32 s11, s35, s11
	s_add_i32 s6, s7, s30
	v_mfma_f32_32x32x16_bf16 v[82:97], v[218:221], v[106:109], v[82:97]
	s_add_i32 s6, s6, s8
	s_add_i32 m0, s6, 0x1a000
	s_nop 0
	global_load_lds_dwordx4 v232, s[10:11]
	v_mfma_f32_32x32x16_bf16 v[82:97], v[226:229], v[102:105], v[82:97]
	s_add_i32 m0, s6, 0x1a400
	v_mfma_f32_32x32x16_bf16 v[82:97], v[186:189], v[98:101], v[82:97]
	global_load_lds_dwordx4 v251, s[10:11]
	s_add_i32 m0, s6, 0x1a800
	s_waitcnt lgkmcnt(0)
	v_mfma_f32_32x32x16_bf16 v[82:97], v[246:249], v[198:201], v[82:97]
	v_mfma_f32_32x32x16_bf16 v[82:97], v[242:245], v[206:209], v[82:97]
	global_load_lds_dwordx4 v252, s[10:11]
	v_mfma_f32_32x32x16_bf16 v[82:97], v[238:241], v[214:217], v[82:97]
	v_mfma_f32_32x32x16_bf16 v[82:97], v[234:237], v[222:225], v[82:97]
	v_exp_f32_e32 v194, v130
	v_add_f32_e32 v130, 0, v178
	v_add_f32_e32 v130, v182, v130
	v_add_f32_e32 v130, v179, v130
	v_add_f32_e32 v130, v183, v130
	v_add_f32_e32 v130, v180, v130
	v_add_f32_e32 v130, v184, v130
	v_add_f32_e32 v130, v177, v130
	v_add_f32_e32 v130, v181, v130
	v_add_f32_e32 v130, v171, v130
	v_add_f32_e32 v130, v175, v130
	v_add_f32_e32 v130, v172, v130
	v_add_f32_e32 v130, v176, v130
	v_exp_f32_e32 v146, v146
	v_add_f32_e32 v130, v168, v130
	v_exp_f32_e32 v147, v147
	v_add_f32_e32 v130, v173, v130
	v_exp_f32_e32 v167, v144
	v_add_f32_e32 v130, v169, v130
	v_exp_f32_e32 v185, v145
	v_add_f32_e32 v130, v174, v130
	v_exp_f32_e32 v186, v142
	v_add_f32_e32 v130, v146, v130
	v_exp_f32_e32 v187, v143
	v_add_f32_e32 v130, v147, v130
	v_exp_f32_e32 v188, v140
	v_add_f32_e32 v130, v167, v130
	v_exp_f32_e32 v189, v141
	v_add_f32_e32 v130, v185, v130
	v_exp_f32_e32 v190, v138
	v_add_f32_e32 v130, v186, v130
	v_exp_f32_e32 v191, v139
	v_add_f32_e32 v130, v187, v130
	v_exp_f32_e32 v192, v136
	v_add_f32_e32 v130, v188, v130
	v_exp_f32_e32 v193, v137
	v_add_f32_e32 v130, v189, v130
	v_exp_f32_e32 v132, v132
	v_add_f32_e32 v130, v190, v130
	v_exp_f32_e32 v133, v133
	v_add_f32_e32 v130, v191, v130
	v_add_f32_e32 v130, v192, v130
	v_exp_f32_e32 v195, v131
	v_add_f32_e32 v130, v193, v130
	v_add_f32_e32 v130, v132, v130
	v_add_f32_e32 v130, v133, v130
	v_add_f32_e32 v130, v194, v130
	v_add_f32_e32 v136, v195, v130
	v_mov_b32_e32 v137, v136
	v_cvt_pk_bf16_f32 v138, v178, v182
	v_cvt_pk_bf16_f32 v139, v179, v183
	v_cvt_pk_bf16_f32 v140, v180, v184
	v_cvt_pk_bf16_f32 v141, v177, v181
	v_cvt_pk_bf16_f32 v142, v171, v175
	v_cvt_pk_bf16_f32 v143, v172, v176
	v_cvt_pk_bf16_f32 v144, v168, v173
	v_cvt_pk_bf16_f32 v145, v169, v174
	v_cvt_pk_bf16_f32 v166, v146, v147
	v_cvt_pk_bf16_f32 v167, v167, v185
	v_cvt_pk_bf16_f32 v168, v186, v187
	v_cvt_pk_bf16_f32 v169, v188, v189
	s_nop 1
	v_permlane32_swap_b32_e32 v136, v137
	v_permlane32_swap_b32_e32 v138, v140
	v_permlane32_swap_b32_e32 v167, v169
	v_cvt_pk_bf16_f32 v130, v190, v191
	v_cvt_pk_bf16_f32 v131, v192, v193
	v_cvt_pk_bf16_f32 v132, v132, v133
	v_cvt_pk_bf16_f32 v133, v194, v195
	v_permlane32_swap_b32_e32 v139, v141
	v_permlane32_swap_b32_e32 v142, v144
	v_permlane32_swap_b32_e32 v143, v145
	v_permlane32_swap_b32_e32 v166, v168
	v_permlane32_swap_b32_e32 v130, v132
	v_permlane32_swap_b32_e32 v131, v133
	ds_read_b64_tr_b16 v[172:173], v160 offset:0
	ds_read_b64_tr_b16 v[174:175], v160 offset:0x800
	ds_read_b64_tr_b16 v[176:177], v160 offset:0x1000
	ds_read_b64_tr_b16 v[178:179], v160 offset:0x1800
	ds_read_b64_tr_b16 v[180:181], v160 offset:0x2000
	ds_read_b64_tr_b16 v[182:183], v160 offset:0x2800
	ds_read_b64_tr_b16 v[184:185], v160 offset:0x3000
	ds_read_b64_tr_b16 v[186:187], v160 offset:0x3800
	s_nop 0
	s_waitcnt lgkmcnt(4)
	v_mfma_f32_32x32x16_bf16 v[2:17], v[138:141], v[172:175], v[2:17]
	ds_read_b64_tr_b16 v[172:173], v160 offset:0x200
	ds_read_b64_tr_b16 v[174:175], v160 offset:0xa00
	v_mfma_f32_32x32x16_bf16 v[2:17], v[142:145], v[176:179], v[2:17]
	ds_read_b64_tr_b16 v[176:177], v160 offset:0x1200
	ds_read_b64_tr_b16 v[178:179], v160 offset:0x1a00
	s_waitcnt lgkmcnt(4)
	v_mfma_f32_32x32x16_bf16 v[2:17], v[166:169], v[180:183], v[2:17]
	ds_read_b64_tr_b16 v[180:181], v160 offset:0x2200
	ds_read_b64_tr_b16 v[182:183], v160 offset:0x2a00
	ds_read_b64_tr_b16 v[188:189], v160 offset:0x3200
	ds_read_b64_tr_b16 v[190:191], v160 offset:0x3a00
	v_mfma_f32_32x32x16_bf16 v[2:17], v[130:133], v[184:187], v[2:17]
	s_waitcnt lgkmcnt(4)
	v_mfma_f32_32x32x16_bf16 v[50:65], v[138:141], v[172:175], v[50:65]
	ds_read_b64_tr_b16 v[172:173], v160 offset:0x400
	ds_read_b64_tr_b16 v[174:175], v160 offset:0xc00
	v_mfma_f32_32x32x16_bf16 v[50:65], v[142:145], v[176:179], v[50:65]
	ds_read_b64_tr_b16 v[176:177], v160 offset:0x1400
	ds_read_b64_tr_b16 v[178:179], v160 offset:0x1c00
	s_waitcnt lgkmcnt(4)
	v_mfma_f32_32x32x16_bf16 v[50:65], v[166:169], v[180:183], v[50:65]
	ds_read_b64_tr_b16 v[180:181], v160 offset:0x2400
	ds_read_b64_tr_b16 v[182:183], v160 offset:0x2c00
	ds_read_b64_tr_b16 v[184:185], v160 offset:0x3400
	ds_read_b64_tr_b16 v[186:187], v160 offset:0x3c00
	v_mfma_f32_32x32x16_bf16 v[50:65], v[130:133], v[188:191], v[50:65]
	s_waitcnt lgkmcnt(4)
	v_mfma_f32_32x32x16_bf16 v[34:49], v[138:141], v[172:175], v[34:49]
	ds_read_b64_tr_b16 v[172:173], v160 offset:0x600
	ds_read_b64_tr_b16 v[174:175], v160 offset:0xe00
	v_mfma_f32_32x32x16_bf16 v[34:49], v[142:145], v[176:179], v[34:49]
	ds_read_b64_tr_b16 v[176:177], v160 offset:0x1600
	ds_read_b64_tr_b16 v[178:179], v160 offset:0x1e00
	s_waitcnt lgkmcnt(4)
	v_mfma_f32_32x32x16_bf16 v[34:49], v[166:169], v[180:183], v[34:49]
	ds_read_b64_tr_b16 v[180:181], v160 offset:0x2600
	ds_read_b64_tr_b16 v[182:183], v160 offset:0x2e00
	ds_read_b64_tr_b16 v[188:189], v160 offset:0x3600
	ds_read_b64_tr_b16 v[190:191], v160 offset:0x3e00
	v_mfma_f32_32x32x16_bf16 v[34:49], v[130:133], v[184:187], v[34:49]
	v_max_f32_e32 v146, v67, v67
	v_max_f32_e32 v147, v66, v66
	v_max_f32_e32 v146, v147, v146
	v_max3_f32 v146, v146, v68, v69
	v_max3_f32 v146, v146, v70, v71
	s_waitcnt lgkmcnt(4)
	v_mfma_f32_32x32x16_bf16 v[18:33], v[138:141], v[172:175], v[18:33]
	v_max3_f32 v138, v146, v72, v73
	v_max3_f32 v138, v138, v74, v75
	v_max3_f32 v138, v138, v76, v77
	v_max3_f32 v138, v138, v78, v79
	v_max3_f32 v138, v138, v80, v81
	v_max3_f32 v138, v138, v82, v83
	v_max3_f32 v138, v138, v84, v85
	v_max3_f32 v138, v138, v86, v87
	v_max3_f32 v138, v138, v88, v89
	v_max3_f32 v138, v138, v90, v91
	v_max3_f32 v138, v138, v92, v93
	v_max3_f32 v138, v138, v94, v95
	v_max3_f32 v138, v138, v96, v97
	v_mov_b32_e32 v139, v138
	s_nop 1
	v_permlane32_swap_b32_e32 v138, v139
	v_max_f32_e32 v139, v139, v139
	v_max_f32_e32 v138, v138, v138
	v_max_f32_e32 v138, v138, v139
	v_sub_f32_e32 v139, v138, v165
	v_mfma_f32_32x32x16_bf16 v[18:33], v[142:145], v[176:179], v[18:33]
	v_cmp_ge_f32_e32 vcc, s65, v139
	s_waitcnt vmcnt(3) lgkmcnt(0)
	s_barrier
	s_cmp_eq_u64 vcc, exec
	s_cselect_b64 s[6:7], -1, 0
	s_cmp_lt_u32 s78, 4
	s_cselect_b32 s12, s74, s15
	s_add_i32 s12, s12, s9
	s_mul_hi_i32 s13, s12, 0x1080
	s_mulk_i32 s12, 0x1080
	s_add_u32 s12, s3, s12
	s_mov_b32 m0, s70
	s_addc_u32 s13, s35, s13
	global_load_lds_dwordx4 v253, s[12:13]
	s_mov_b32 m0, s72
	v_mfma_f32_32x32x16_bf16 v[18:33], v[166:169], v[180:183], v[18:33]
	global_load_lds_dwordx4 v254, s[12:13]
	v_max_f32_e32 v139, v165, v165
	v_max_f32_e32 v138, v139, v138
	v_sub_f32_e32 v139, v165, v138
	v_mul_f32_e32 v139, 0x3dd53b94, v139
	v_exp_f32_e32 v139, v139
	v_mfma_f32_32x32x16_bf16 v[18:33], v[130:133], v[188:191], v[18:33]
	v_cndmask_b32_e64 v167, v139, 1.0, s[6:7]
	v_cmp_gt_f32_e32 vcc, 1.0, v167
	s_cbranch_vccz .LBB0_1177
	s_and_saveexec_b64 s[12:13], s[4:5]
	ds_write_b32 v155, v167 offset:128
	s_or_b64 exec, exec, s[12:13]
	s_waitcnt lgkmcnt(0)
	v_add_u32_e32 v139, s69, v134
	ds_read_b128 v[130:133], v139 offset:224
	ds_read_b128 v[140:143], v139 offset:192
	ds_read_b128 v[144:147], v139 offset:160
	ds_read_b128 v[172:175], v139 offset:128
	s_waitcnt lgkmcnt(0)
	v_pk_mul_f32 v[14:15], v[14:15], v[130:131]
	v_pk_mul_f32 v[10:11], v[10:11], v[140:141]
	v_pk_mul_f32 v[6:7], v[6:7], v[144:145]
	v_pk_mul_f32 v[16:17], v[16:17], v[132:133]
	v_pk_mul_f32 v[12:13], v[12:13], v[142:143]
	v_pk_mul_f32 v[8:9], v[8:9], v[146:147]
	v_pk_mul_f32 v[4:5], v[4:5], v[174:175]
	v_pk_mul_f32 v[2:3], v[2:3], v[172:173]
	v_pk_mul_f32 v[62:63], v[62:63], v[130:131]
	v_pk_mul_f32 v[58:59], v[58:59], v[140:141]
	v_pk_mul_f32 v[54:55], v[54:55], v[144:145]
	v_pk_mul_f32 v[64:65], v[64:65], v[132:133]
	v_pk_mul_f32 v[60:61], v[60:61], v[142:143]
	v_pk_mul_f32 v[56:57], v[56:57], v[146:147]
	v_pk_mul_f32 v[52:53], v[52:53], v[174:175]
	v_pk_mul_f32 v[50:51], v[50:51], v[172:173]
	v_pk_mul_f32 v[46:47], v[46:47], v[130:131]
	v_pk_mul_f32 v[42:43], v[42:43], v[140:141]
	v_pk_mul_f32 v[38:39], v[38:39], v[144:145]
	v_pk_mul_f32 v[48:49], v[48:49], v[132:133]
	v_pk_mul_f32 v[44:45], v[44:45], v[142:143]
	v_pk_mul_f32 v[40:41], v[40:41], v[146:147]
	v_pk_mul_f32 v[36:37], v[36:37], v[174:175]
	v_pk_mul_f32 v[34:35], v[34:35], v[172:173]
	v_pk_mul_f32 v[30:31], v[30:31], v[130:131]
	v_pk_mul_f32 v[26:27], v[26:27], v[140:141]
	v_pk_mul_f32 v[22:23], v[22:23], v[144:145]
	v_pk_mul_f32 v[32:33], v[32:33], v[132:133]
	v_pk_mul_f32 v[28:29], v[28:29], v[142:143]
	v_pk_mul_f32 v[24:25], v[24:25], v[146:147]
	v_pk_mul_f32 v[20:21], v[20:21], v[174:175]
	v_pk_mul_f32 v[18:19], v[18:19], v[172:173]
.LBB0_1177:
	v_cndmask_b32_e64 v130, v138, v165, s[6:7]
	s_mul_hi_u32 s12, s79, 0xaaaaaaab
	v_mul_f32_e32 v131, 0xbdd53b94, v130
	s_lshr_b32 s12, s12, 1
	v_fmamk_f32 v66, v66, 0x3dd53b94, v131
	v_fmamk_f32 v68, v68, 0x3dd53b94, v131
	v_fmamk_f32 v70, v70, 0x3dd53b94, v131
	v_fmamk_f32 v72, v72, 0x3dd53b94, v131
	s_mul_i32 s12, s12, 0xfffee000
	v_fmamk_f32 v74, v74, 0x3dd53b94, v131
	v_fmamk_f32 v76, v76, 0x3dd53b94, v131
	v_fmamk_f32 v78, v78, 0x3dd53b94, v131
	v_fmamk_f32 v80, v80, 0x3dd53b94, v131
	v_fmamk_f32 v132, v82, 0x3dd53b94, v131
	v_fmamk_f32 v133, v84, 0x3dd53b94, v131
	v_fmamk_f32 v146, v86, 0x3dd53b94, v131
	v_fmamk_f32 v147, v88, 0x3dd53b94, v131
	v_fmamk_f32 v165, v90, 0x3dd53b94, v131
	v_fmamk_f32 v166, v92, 0x3dd53b94, v131
	v_fmamk_f32 v168, v94, 0x3dd53b94, v131
	v_fmamk_f32 v169, v96, 0x3dd53b94, v131
	v_exp_f32_e32 v171, v66
	v_exp_f32_e32 v224, v68
	v_exp_f32_e32 v225, v70
	v_exp_f32_e32 v226, v72
	v_fmamk_f32 v66, v67, 0x3dd53b94, v131
	v_fmamk_f32 v67, v69, 0x3dd53b94, v131
	v_fmamk_f32 v68, v71, 0x3dd53b94, v131
	v_fmamk_f32 v69, v73, 0x3dd53b94, v131
	v_fmamk_f32 v70, v75, 0x3dd53b94, v131
	v_fmamk_f32 v71, v77, 0x3dd53b94, v131
	v_fmamk_f32 v72, v79, 0x3dd53b94, v131
	v_fmamk_f32 v73, v81, 0x3dd53b94, v131
	v_fmamk_f32 v231, v83, 0x3dd53b94, v131
	v_fmamk_f32 v233, v85, 0x3dd53b94, v131
	v_fmamk_f32 v234, v87, 0x3dd53b94, v131
	v_fmamk_f32 v235, v89, 0x3dd53b94, v131
	v_fmamk_f32 v236, v91, 0x3dd53b94, v131
	v_fmamk_f32 v245, v93, 0x3dd53b94, v131
	v_fmamk_f32 v246, v95, 0x3dd53b94, v131
	v_fmac_f32_e32 v131, 0x3dd53b94, v97
	v_exp_f32_e32 v227, v74
	v_exp_f32_e32 v228, v76
	v_exp_f32_e32 v229, v78
	v_exp_f32_e32 v230, v80
	v_exp_f32_e32 v237, v66
	v_exp_f32_e32 v238, v67
	v_exp_f32_e32 v239, v68
	v_exp_f32_e32 v240, v69
	v_exp_f32_e32 v241, v70
	v_exp_f32_e32 v242, v71
	v_exp_f32_e32 v243, v72
	v_exp_f32_e32 v244, v73
	v_add_u32_e32 v196, s16, v159
	v_add_u32_e32 v204, s16, v161
	v_add_u32_e32 v212, s16, v162
	v_add_u32_e32 v220, s16, v163
	ds_read_b128 v[66:69], v196 offset:32768
	ds_read_b128 v[82:85], v204 offset:32768
	ds_read_b128 v[86:89], v212 offset:32768
	ds_read_b128 v[90:93], v220 offset:32768
	ds_read_b128 v[94:97], v196 offset:32896
	ds_read_b128 v[138:141], v204 offset:32896
	ds_read_b128 v[142:145], v212 offset:32896
	ds_read_b128 v[172:175], v220 offset:32896
	ds_read_b128 v[176:179], v158
	ds_read_b128 v[180:183], v196 offset:33024
	ds_read_b128 v[184:187], v158 offset:1024
	ds_read_b128 v[188:191], v204 offset:33024
	ds_read_b128 v[192:195], v158 offset:2048
	ds_read_b128 v[200:203], v212 offset:33024
	ds_read_b128 v[208:211], v158 offset:3072
	s_waitcnt lgkmcnt(14)
	v_mfma_f32_32x32x16_bf16 v[66:81], v[66:69], v[126:129], 0
	ds_read_b128 v[216:219], v220 offset:33024
	s_waitcnt lgkmcnt(11)
	v_mfma_f32_32x32x16_bf16 v[66:81], v[82:85], v[122:125], v[66:81]
	v_mfma_f32_32x32x16_bf16 v[66:81], v[86:89], v[118:121], v[66:81]
	v_mfma_f32_32x32x16_bf16 v[66:81], v[90:93], v[114:117], v[66:81]
	v_mfma_f32_32x32x16_bf16 v[66:81], v[94:97], v[110:113], v[66:81]
	s_waitcnt lgkmcnt(8)
	v_mfma_f32_32x32x16_bf16 v[66:81], v[138:141], v[106:109], v[66:81]
	ds_read_b128 v[138:141], v196 offset:45056
	v_mfma_f32_32x32x16_bf16 v[66:81], v[142:145], v[102:105], v[66:81]
	ds_read_b128 v[142:145], v204 offset:45056
	v_mfma_f32_32x32x16_bf16 v[66:81], v[172:175], v[98:101], v[66:81]
	ds_read_b128 v[172:175], v212 offset:45056
	s_waitcnt lgkmcnt(3)
	v_mfma_f32_32x32x16_bf16 v[66:81], v[180:183], v[176:179], v[66:81]
	ds_read_b128 v[180:183], v220 offset:45056
	v_mfma_f32_32x32x16_bf16 v[66:81], v[188:191], v[184:187], v[66:81]
	ds_read_b128 v[188:191], v196 offset:45184
	v_mfma_f32_32x32x16_bf16 v[66:81], v[200:203], v[192:195], v[66:81]
	ds_read_b128 v[200:203], v204 offset:45184
	v_mfma_f32_32x32x16_bf16 v[66:81], v[216:219], v[208:211], v[66:81]
	ds_read_b128 v[216:219], v212 offset:45184
	s_waitcnt lgkmcnt(3)
	v_mfma_f32_32x32x16_bf16 v[82:97], v[138:141], v[126:129], 0
	ds_read_b128 v[138:141], v220 offset:45184
	s_add_i32 s78, s78, 2
	s_min_u32 s6, s78, s14
	s_lshl_b32 s7, s6, 6
	s_cmp_lt_u32 s6, 4
	s_cselect_b32 s6, s74, s15
	s_add_i32 s6, s6, s7
	s_mul_hi_i32 s7, s6, 0x1080
	v_mfma_f32_32x32x16_bf16 v[82:97], v[142:145], v[122:125], v[82:97]
	ds_read_b128 v[196:199], v196 offset:45312
	s_mulk_i32 s6, 0x1080
	v_mfma_f32_32x32x16_bf16 v[82:97], v[172:175], v[118:121], v[82:97]
	ds_read_b128 v[204:207], v204 offset:45312
	v_mfma_f32_32x32x16_bf16 v[82:97], v[180:183], v[114:117], v[82:97]
	ds_read_b128 v[212:215], v212 offset:45312
	s_waitcnt lgkmcnt(3)
	v_mfma_f32_32x32x16_bf16 v[82:97], v[188:191], v[110:113], v[82:97]
	ds_read_b128 v[220:223], v220 offset:45312
	s_add_u32 s6, s3, s6
	s_addc_u32 s7, s35, s7
	s_add_i32 s12, s12, s30
	v_mfma_f32_32x32x16_bf16 v[82:97], v[200:203], v[106:109], v[82:97]
	s_add_i32 s12, s12, s8
	s_add_i32 m0, s12, 0x20000
	s_nop 0
	global_load_lds_dwordx4 v232, s[6:7]
	v_mfma_f32_32x32x16_bf16 v[82:97], v[216:219], v[102:105], v[82:97]
	s_add_i32 m0, s12, 0x20400
	v_mfma_f32_32x32x16_bf16 v[82:97], v[138:141], v[98:101], v[82:97]
	global_load_lds_dwordx4 v251, s[6:7]
	s_add_i32 m0, s12, 0x20800
	s_waitcnt lgkmcnt(0)
	v_mfma_f32_32x32x16_bf16 v[82:97], v[196:199], v[176:179], v[82:97]
	v_mfma_f32_32x32x16_bf16 v[82:97], v[204:207], v[184:187], v[82:97]
	global_load_lds_dwordx4 v252, s[6:7]
	v_mfma_f32_32x32x16_bf16 v[82:97], v[212:215], v[192:195], v[82:97]
	v_mfma_f32_32x32x16_bf16 v[82:97], v[220:223], v[208:211], v[82:97]
	v_add_f32_e32 v138, 0, v171
	v_add_f32_e32 v138, v237, v138
	v_add_f32_e32 v138, v224, v138
	v_add_f32_e32 v138, v238, v138
	v_add_f32_e32 v138, v225, v138
	v_add_f32_e32 v138, v239, v138
	v_add_f32_e32 v138, v226, v138
	v_add_f32_e32 v138, v240, v138
	v_add_f32_e32 v138, v227, v138
	v_add_f32_e32 v138, v241, v138
	v_add_f32_e32 v138, v228, v138
	v_add_f32_e32 v138, v242, v138
	v_exp_f32_e32 v132, v132
	v_add_f32_e32 v138, v229, v138
	v_exp_f32_e32 v172, v231
	v_add_f32_e32 v138, v243, v138
	v_exp_f32_e32 v133, v133
	v_add_f32_e32 v138, v230, v138
	v_exp_f32_e32 v173, v233
	v_add_f32_e32 v138, v244, v138
	v_exp_f32_e32 v146, v146
	v_add_f32_e32 v138, v132, v138
	v_exp_f32_e32 v174, v234
	v_add_f32_e32 v138, v172, v138
	v_exp_f32_e32 v147, v147
	v_add_f32_e32 v138, v133, v138
	v_exp_f32_e32 v175, v235
	v_add_f32_e32 v138, v173, v138
	v_exp_f32_e32 v165, v165
	v_add_f32_e32 v138, v146, v138
	v_exp_f32_e32 v176, v236
	v_add_f32_e32 v138, v174, v138
	v_exp_f32_e32 v166, v166
	v_add_f32_e32 v138, v147, v138
	v_exp_f32_e32 v177, v245
	v_add_f32_e32 v138, v175, v138
	v_exp_f32_e32 v168, v168
	v_add_f32_e32 v138, v165, v138
	v_exp_f32_e32 v178, v246
	v_add_f32_e32 v138, v176, v138
	v_exp_f32_e32 v169, v169
	v_add_f32_e32 v138, v166, v138
	v_exp_f32_e32 v131, v131
	v_add_f32_e32 v138, v177, v138
	v_add_f32_e32 v138, v168, v138
	v_add_f32_e32 v138, v178, v138
	v_add_f32_e32 v138, v169, v138
	v_add_f32_e32 v185, v131, v138
	v_mov_b32_e32 v186, v185
	s_nop 1
	v_permlane32_swap_b32_e32 v185, v186
	v_cvt_pk_bf16_f32 v138, v171, v237
	v_cvt_pk_bf16_f32 v139, v224, v238
	v_cvt_pk_bf16_f32 v140, v225, v239
	v_cvt_pk_bf16_f32 v141, v226, v240
	v_cvt_pk_bf16_f32 v142, v227, v241
	v_cvt_pk_bf16_f32 v143, v228, v242
	v_cvt_pk_bf16_f32 v144, v229, v243
	v_cvt_pk_bf16_f32 v145, v230, v244
	v_cvt_pk_bf16_f32 v172, v132, v172
	v_cvt_pk_bf16_f32 v173, v133, v173
	v_cvt_pk_bf16_f32 v174, v146, v174
	v_cvt_pk_bf16_f32 v175, v147, v175
	v_cvt_pk_bf16_f32 v176, v165, v176
	v_cvt_pk_bf16_f32 v177, v166, v177
	v_cvt_pk_bf16_f32 v178, v168, v178
	v_cvt_pk_bf16_f32 v179, v169, v131
	s_nop 0
	v_permlane32_swap_b32_e32 v138, v140
	v_permlane32_swap_b32_e32 v139, v141
	v_permlane32_swap_b32_e32 v142, v144
	v_permlane32_swap_b32_e32 v143, v145
	v_permlane32_swap_b32_e32 v172, v174
	v_permlane32_swap_b32_e32 v173, v175
	v_permlane32_swap_b32_e32 v176, v178
	v_permlane32_swap_b32_e32 v177, v179
	ds_read_b64_tr_b16 v[180:181], v156 offset:0
	ds_read_b64_tr_b16 v[182:183], v156 offset:0x800
	ds_read_b64_tr_b16 v[188:189], v156 offset:0x1000
	ds_read_b64_tr_b16 v[190:191], v156 offset:0x1800
	ds_read_b64_tr_b16 v[192:193], v156 offset:0x2000
	ds_read_b64_tr_b16 v[194:195], v156 offset:0x2800
	ds_read_b64_tr_b16 v[196:197], v156 offset:0x3000
	ds_read_b64_tr_b16 v[198:199], v156 offset:0x3800
	s_nop 0
	s_waitcnt lgkmcnt(4)
	v_mfma_f32_32x32x16_bf16 v[2:17], v[138:141], v[180:183], v[2:17]
	ds_read_b64_tr_b16 v[180:181], v156 offset:0x200
	ds_read_b64_tr_b16 v[182:183], v156 offset:0xa00
	v_mfma_f32_32x32x16_bf16 v[2:17], v[142:145], v[188:191], v[2:17]
	ds_read_b64_tr_b16 v[188:189], v156 offset:0x1200
	ds_read_b64_tr_b16 v[190:191], v156 offset:0x1a00
	s_waitcnt lgkmcnt(4)
	v_mfma_f32_32x32x16_bf16 v[2:17], v[172:175], v[192:195], v[2:17]
	ds_read_b64_tr_b16 v[192:193], v156 offset:0x2200
	ds_read_b64_tr_b16 v[194:195], v156 offset:0x2a00
	ds_read_b64_tr_b16 v[200:201], v156 offset:0x3200
	ds_read_b64_tr_b16 v[202:203], v156 offset:0x3a00
	v_mfma_f32_32x32x16_bf16 v[2:17], v[176:179], v[196:199], v[2:17]
	s_waitcnt lgkmcnt(4)
	v_mfma_f32_32x32x16_bf16 v[50:65], v[138:141], v[180:183], v[50:65]
	ds_read_b64_tr_b16 v[180:181], v156 offset:0x400
	ds_read_b64_tr_b16 v[182:183], v156 offset:0xc00
	v_mfma_f32_32x32x16_bf16 v[50:65], v[142:145], v[188:191], v[50:65]
	ds_read_b64_tr_b16 v[188:189], v156 offset:0x1400
	ds_read_b64_tr_b16 v[190:191], v156 offset:0x1c00
	s_waitcnt lgkmcnt(4)
	v_mfma_f32_32x32x16_bf16 v[50:65], v[172:175], v[192:195], v[50:65]
	ds_read_b64_tr_b16 v[192:193], v156 offset:0x2400
	ds_read_b64_tr_b16 v[194:195], v156 offset:0x2c00
	ds_read_b64_tr_b16 v[196:197], v156 offset:0x3400
	ds_read_b64_tr_b16 v[198:199], v156 offset:0x3c00
	v_mfma_f32_32x32x16_bf16 v[50:65], v[176:179], v[200:203], v[50:65]
	s_waitcnt lgkmcnt(4)
	v_mfma_f32_32x32x16_bf16 v[34:49], v[138:141], v[180:183], v[34:49]
	ds_read_b64_tr_b16 v[180:181], v156 offset:0x600
	ds_read_b64_tr_b16 v[182:183], v156 offset:0xe00
	v_mfma_f32_32x32x16_bf16 v[34:49], v[142:145], v[188:191], v[34:49]
	ds_read_b64_tr_b16 v[188:189], v156 offset:0x1600
	ds_read_b64_tr_b16 v[190:191], v156 offset:0x1e00
	s_waitcnt lgkmcnt(4)
	v_mfma_f32_32x32x16_bf16 v[34:49], v[172:175], v[192:195], v[34:49]
	ds_read_b64_tr_b16 v[192:193], v156 offset:0x2600
	ds_read_b64_tr_b16 v[194:195], v156 offset:0x2e00
	ds_read_b64_tr_b16 v[200:201], v156 offset:0x3600
	ds_read_b64_tr_b16 v[202:203], v156 offset:0x3e00
	v_mfma_f32_32x32x16_bf16 v[34:49], v[176:179], v[196:199], v[34:49]
	s_waitcnt vmcnt(3) lgkmcnt(0)
	s_barrier
	v_mfma_f32_32x32x16_bf16 v[18:33], v[138:141], v[180:183], v[18:33]
	s_mov_b32 m0, s76
	s_nop 0
	global_load_lds_dwordx4 v253, s[10:11]
	s_mov_b32 m0, s77
	v_max_f32_e32 v132, v66, v66
	global_load_lds_dwordx4 v254, s[10:11]
	v_max_f32_e32 v131, v67, v67
	v_max_f32_e32 v131, v132, v131
	v_max3_f32 v131, v131, v68, v69
	v_max3_f32 v131, v131, v70, v71
	v_max3_f32 v131, v131, v72, v73
	v_max3_f32 v131, v131, v74, v75
	v_mfma_f32_32x32x16_bf16 v[18:33], v[142:145], v[188:191], v[18:33]
	v_max3_f32 v131, v131, v76, v77
	v_max3_f32 v131, v131, v78, v79
	v_max3_f32 v131, v131, v80, v81
	v_max3_f32 v131, v131, v82, v83
	v_max3_f32 v131, v131, v84, v85
	v_max3_f32 v131, v131, v86, v87
	v_max3_f32 v131, v131, v88, v89
	v_max3_f32 v131, v131, v90, v91
	v_mfma_f32_32x32x16_bf16 v[18:33], v[172:175], v[192:195], v[18:33]
	v_max3_f32 v131, v131, v92, v93
	v_max3_f32 v131, v131, v94, v95
	v_max3_f32 v131, v131, v96, v97
	v_mov_b32_e32 v132, v131
	s_nop 1
	v_permlane32_swap_b32_e32 v131, v132
	v_max_f32_e32 v132, v132, v132
	v_max_f32_e32 v131, v131, v131
	v_max_f32_e32 v131, v131, v132
	v_max_f32_e32 v133, v130, v130
	v_sub_f32_e32 v132, v131, v130
	v_max_f32_e32 v131, v133, v131
	v_mfma_f32_32x32x16_bf16 v[18:33], v[176:179], v[200:203], v[18:33]
	v_sub_f32_e32 v133, v130, v131
	v_mul_f32_e32 v133, 0x3dd53b94, v133
	v_exp_f32_e32 v133, v133
	v_cmp_ge_f32_e32 vcc, s65, v132
	s_cmp_eq_u64 vcc, exec
	s_cselect_b64 s[6:7], -1, 0
	v_cndmask_b32_e64 v166, v133, 1.0, s[6:7]
	v_cmp_gt_f32_e32 vcc, 1.0, v166
	s_cbranch_vccz .LBB0_1181
	s_and_saveexec_b64 s[10:11], s[4:5]
	ds_write_b32 v155, v166 offset:128
	s_or_b64 exec, exec, s[10:11]
	s_waitcnt lgkmcnt(0)
	v_add_u32_e32 v132, s69, v134
	ds_read_b128 v[138:141], v132 offset:224
	ds_read_b128 v[142:145], v132 offset:192
	ds_read_b128 v[172:175], v132 offset:160
	ds_read_b128 v[176:179], v132 offset:128
	s_waitcnt lgkmcnt(0)
	v_pk_mul_f32 v[14:15], v[14:15], v[138:139]
	v_pk_mul_f32 v[10:11], v[10:11], v[142:143]
	v_pk_mul_f32 v[6:7], v[6:7], v[172:173]
	v_pk_mul_f32 v[16:17], v[16:17], v[140:141]
	v_pk_mul_f32 v[12:13], v[12:13], v[144:145]
	v_pk_mul_f32 v[8:9], v[8:9], v[174:175]
	v_pk_mul_f32 v[4:5], v[4:5], v[178:179]
	v_pk_mul_f32 v[2:3], v[2:3], v[176:177]
	v_pk_mul_f32 v[62:63], v[62:63], v[138:139]
	v_pk_mul_f32 v[58:59], v[58:59], v[142:143]
	v_pk_mul_f32 v[54:55], v[54:55], v[172:173]
	v_pk_mul_f32 v[64:65], v[64:65], v[140:141]
	v_pk_mul_f32 v[60:61], v[60:61], v[144:145]
	v_pk_mul_f32 v[56:57], v[56:57], v[174:175]
	v_pk_mul_f32 v[52:53], v[52:53], v[178:179]
	v_pk_mul_f32 v[50:51], v[50:51], v[176:177]
	v_pk_mul_f32 v[46:47], v[46:47], v[138:139]
	v_pk_mul_f32 v[42:43], v[42:43], v[142:143]
	v_pk_mul_f32 v[38:39], v[38:39], v[172:173]
	v_pk_mul_f32 v[48:49], v[48:49], v[140:141]
	v_pk_mul_f32 v[44:45], v[44:45], v[144:145]
	v_pk_mul_f32 v[40:41], v[40:41], v[174:175]
	v_pk_mul_f32 v[36:37], v[36:37], v[178:179]
	v_pk_mul_f32 v[34:35], v[34:35], v[176:177]
	v_pk_mul_f32 v[30:31], v[30:31], v[138:139]
	v_pk_mul_f32 v[26:27], v[26:27], v[142:143]
	v_pk_mul_f32 v[22:23], v[22:23], v[172:173]
	v_pk_mul_f32 v[32:33], v[32:33], v[140:141]
	v_pk_mul_f32 v[28:29], v[28:29], v[144:145]
	v_pk_mul_f32 v[24:25], v[24:25], v[174:175]
	v_pk_mul_f32 v[20:21], v[20:21], v[178:179]
	v_pk_mul_f32 v[18:19], v[18:19], v[176:177]

.LBB0_3030:
	v_readlane_b32 s4, v255, 4
	v_readlane_b32 s5, v255, 5
	s_lshl_b64 s[4:5], s[4:5], 2
	v_readlane_b32 s6, v255, 2
	s_add_u32 s6, s6, s4
	v_readlane_b32 s4, v255, 3
	s_addc_u32 s7, s4, s5
	v_readlane_b32 s4, v255, 6
	s_lshl_b32 s4, s4, 8
	s_add_u32 s4, s6, s4
	s_addc_u32 s5, s7, 0
	v_mov_b32_e32 v1, 0x1000
	v_mov_b32_e32 v3, 1
	buffer_inv sc1
	global_atomic_add v3, v1, v3, s[4:5] offset:1024 sc0
	v_cvt_f32_u32_e32 v1, v2
	v_sub_u32_e32 v4, 0, v2
	v_rcp_iflag_f32_e32 v1, v1
	s_nop 0
	v_mul_f32_e32 v1, 0x4f7ffffe, v1
	v_cvt_u32_f32_e32 v1, v1
	v_mul_lo_u32 v4, v4, v1
	v_mul_hi_u32 v4, v1, v4
	v_add_u32_e32 v1, v1, v4
	s_waitcnt vmcnt(0)
	v_mul_hi_u32 v1, v3, v1
	v_mul_lo_u32 v4, v1, v2
	v_sub_u32_e32 v4, v3, v4
	v_add_u32_e32 v5, 1, v1
	v_cmp_ge_u32_e32 vcc, v4, v2
	v_add_u32_e32 v3, 1, v3
	s_nop 0
	v_cndmask_b32_e32 v1, v1, v5, vcc
	v_sub_u32_e32 v5, v4, v2
	v_cndmask_b32_e32 v4, v4, v5, vcc
	v_add_u32_e32 v5, 1, v1
	v_cmp_ge_u32_e32 vcc, v4, v2
	s_nop 1
	v_cndmask_b32_e32 v1, v1, v5, vcc
	v_mul_lo_u32 v4, v2, v1
	v_add_u32_e32 v2, v4, v2
	v_cmp_ne_u32_e32 vcc, v3, v2
	s_and_saveexec_b64 s[8:9], vcc
	s_xor_b64 s[8:9], exec, s[8:9]
	s_cbranch_execz .LBB0_3044
	s_waitcnt lgkmcnt(0)
	v_mov_b32_e32 v0, 0x2000
	global_load_dword v0, v0, s[4:5] offset:1024 sc1
	s_add_u32 s12, s4, 0x2400
	s_addc_u32 s13, s5, 0
	s_waitcnt vmcnt(0)
	v_cmp_eq_u32_e32 vcc, v0, v1
	s_and_saveexec_b64 s[10:11], vcc
	s_cbranch_execz .LBB0_3043
	s_mov_b32 s28, 1
	s_mov_b64 s[14:15], 0
	v_mov_b32_e32 v0, 0
	s_branch .LBB0_3034

.LBB0_3043:
	s_or_b64 exec, exec, s[10:11]
	s_waitcnt vmcnt(0)
	s_waitcnt vmcnt(0)

.LBB0_3061:
	s_or_b64 exec, exec, s[6:7]
	v_mov_b32_e32 v0, 0x2000
	v_mov_b32_e32 v1, 1
	s_waitcnt vmcnt(0)
	global_atomic_add v0, v1, s[4:5] offset:1024
	s_waitcnt vmcnt(0)
